# cache-policy hint: nt on the final-norm output stores (written once, never re-read); on top of v26
# baseline (speedup 1.0000x reference)
.LBB0_1494:
	s_add_u32 s12, s16, s6
	s_addc_u32 s13, s17, s7
	s_nop 2
	global_load_dwordx4 v[42:45], v35, s[12:13]
	global_load_dwordx4 v[46:49], v35, s[12:13] offset:64
	s_add_u32 s2, s12, 0xaa00000
	s_addc_u32 s3, s13, 0
	global_load_dwordx4 v[50:53], v21, s[2:3] offset:16
	global_load_dwordx4 v[54:57], v21, s[2:3] offset:32
	global_load_dwordx4 v[58:61], v21, s[2:3] offset:48
	s_add_u32 s2, s12, 0xaa00040
	s_addc_u32 s3, s13, 0
	global_load_dwordx4 v[64:67], v21, s[2:3] offset:16
	global_load_dwordx4 v[68:71], v21, s[2:3] offset:32
	global_load_dwordx4 v[72:75], v21, s[2:3] offset:48
	v_lshl_add_u64 v[22:23], v[18:19], 0, s[6:7]
	s_add_u32 s2, s12, 0xaa00080
	v_add_co_u32_e32 v26, vcc, 0x6a00000, v22
	s_addc_u32 s3, s13, 0
	s_nop 0
	v_addc_co_u32_e32 v27, vcc, 0, v23, vcc
	global_load_dwordx4 v[76:79], v35, s[12:13] offset:128
	global_load_dwordx2 v[40:41], v[26:27], off
	global_load_dwordx2 v[32:33], v[26:27], off offset:512
	global_load_dwordx2 v[28:29], v[26:27], off offset:1024
	global_load_dwordx2 v[24:25], v[26:27], off offset:1536
	global_load_dwordx4 v[80:83], v21, s[2:3] offset:48
	global_load_dwordx4 v[84:87], v21, s[2:3] offset:32
	global_load_dwordx4 v[88:91], v21, s[2:3] offset:16
	s_waitcnt vmcnt(15)
	v_mov_b32_e32 v30, v43
	v_mov_b32_e32 v31, v44
	v_mov_b32_e32 v43, v45
	v_pk_add_f32 v[30:31], v[30:31], v[42:43]
	s_waitcnt vmcnt(13)
	v_mov_b32_e32 v42, v51
	v_mov_b32_e32 v43, v52
	v_mov_b32_e32 v51, v53
	v_mov_b32_e32 v36, v47
	v_mov_b32_e32 v37, v48
	v_mov_b32_e32 v47, v49
	v_pk_add_f32 v[42:43], v[42:43], v[50:51]
	v_pk_add_f32 v[36:37], v[36:37], v[46:47]
	v_pk_add_f32 v[30:31], v[30:31], v[30:31] op_sel:[0,1] op_sel_hi:[1,0]
	s_waitcnt vmcnt(12)
	v_add_f32_e32 v44, v54, v55
	v_add_f32_e32 v46, v56, v57
	s_waitcnt vmcnt(11)
	v_mov_b32_e32 v45, v60
	v_mov_b32_e32 v47, v61
	v_pk_add_f32 v[42:43], v[42:43], v[42:43] op_sel:[0,1] op_sel_hi:[1,0]
	v_mov_b32_e32 v31, v58
	v_pk_add_f32 v[44:45], v[44:45], v[46:47]
	s_waitcnt vmcnt(10)
	v_mov_b32_e32 v46, v65
	v_mov_b32_e32 v47, v66
	v_mov_b32_e32 v65, v67
	v_mov_b32_e32 v43, v59
	v_pk_add_f32 v[46:47], v[46:47], v[64:65]
	v_pk_add_f32 v[30:31], v[30:31], v[42:43]
	v_pk_add_f32 v[36:37], v[36:37], v[36:37] op_sel:[0,1] op_sel_hi:[1,0]
	v_pk_add_f32 v[42:43], v[46:47], v[46:47] op_sel:[0,1] op_sel_hi:[1,0]
	v_pk_add_f32 v[30:31], v[30:31], v[44:45]
	s_waitcnt vmcnt(9)
	v_add_f32_e32 v48, v68, v69
	v_add_f32_e32 v50, v70, v71
	s_waitcnt vmcnt(8)
	v_mov_b32_e32 v37, v72
	v_mov_b32_e32 v49, v74
	v_mov_b32_e32 v51, v75
	v_mov_b32_e32 v43, v73
	v_add_f32_e32 v20, v30, v31
	v_pk_add_f32 v[48:49], v[48:49], v[50:51]
	v_pk_add_f32 v[30:31], v[36:37], v[42:43]
	v_fmamk_f32 v20, v20, 0x3a800000, v39
	v_pk_add_f32 v[30:31], v[30:31], v[48:49]
	v_mul_f32_e32 v34, 0x4f800000, v20
	v_cmp_gt_f32_e32 vcc, s18, v20
	v_add_f32_e32 v30, v30, v31
	v_fmamk_f32 v30, v30, 0x3a800000, v39
	v_cndmask_b32_e32 v20, v20, v34, vcc
	v_sqrt_f32_e32 v31, v20
	v_mul_f32_e32 v34, 0x4f800000, v30
	v_cmp_gt_f32_e64 s[2:3], s18, v30
	global_load_dwordx4 v[56:59], v35, s[12:13] offset:192
	v_add_u32_e32 v36, -1, v31
	v_cndmask_b32_e64 v30, v30, v34, s[2:3]
	v_sqrt_f32_e32 v34, v30
	v_add_u32_e32 v37, 1, v31
	v_fma_f32 v38, -v36, v31, v20
	v_fma_f32 v42, -v37, v31, v20
	v_cmp_ge_f32_e64 s[4:5], 0, v38
	v_add_u32_e32 v38, 1, v34
	s_nop 0
	v_cndmask_b32_e64 v31, v31, v36, s[4:5]
	v_add_u32_e32 v36, -1, v34
	v_cmp_lt_f32_e64 s[4:5], 0, v42
	v_fma_f32 v42, -v38, v34, v30
	s_nop 0
	v_cndmask_b32_e64 v31, v31, v37, s[4:5]
	v_fma_f32 v37, -v36, v34, v30
	v_mul_f32_e32 v43, 0x37800000, v31
	v_cmp_ge_f32_e64 s[4:5], 0, v37
	v_cndmask_b32_e32 v31, v31, v43, vcc
	v_cmp_lt_f32_e32 vcc, 0, v42
	v_cndmask_b32_e64 v34, v34, v36, s[4:5]
	s_waitcnt vmcnt(2)
	v_add_f32_e32 v42, v86, v87
	v_cndmask_b32_e32 v34, v34, v38, vcc
	v_cmp_class_f32_e32 vcc, v20, v62
	v_mov_b32_e32 v43, v83
	s_nop 0
	v_cndmask_b32_e32 v20, v31, v20, vcc
	v_div_scale_f32 v36, s[4:5], v20, v20, 1.0
	v_rcp_f32_e32 v38, v36
	v_mul_f32_e32 v31, 0x37800000, v34
	v_cndmask_b32_e64 v31, v34, v31, s[2:3]
	v_cmp_class_f32_e64 s[2:3], v30, v62
	v_div_scale_f32 v37, vcc, 1.0, v20, 1.0
	s_nop 0
	v_cndmask_b32_e64 v34, v31, v30, s[2:3]
	v_fma_f32 v30, -v36, v38, 1.0
	v_fmac_f32_e32 v38, v30, v38
	v_mul_f32_e32 v30, v37, v38
	v_fma_f32 v31, -v36, v30, v37
	v_fmac_f32_e32 v30, v31, v38
	v_fma_f32 v31, -v36, v30, v37
	v_div_fmas_f32 v30, v31, v38, v30
	v_div_fixup_f32 v20, v30, v20, 1.0
	v_div_scale_f32 v30, s[2:3], v34, v34, 1.0
	s_add_u32 s2, s12, 0xaa000c0
	s_addc_u32 s3, s13, 0
	s_nop 2
	global_load_dwordx4 v[64:67], v21, s[2:3] offset:16
	global_load_dwordx2 v[92:93], v[26:27], off offset:2048
	global_load_dwordx2 v[94:95], v[26:27], off offset:2560
	global_load_dwordx2 v[60:61], v[26:27], off offset:3072
	global_load_dwordx2 v[52:53], v[26:27], off offset:3584
	global_load_dwordx4 v[68:71], v21, s[2:3] offset:48
	global_load_dwordx4 v[72:75], v21, s[2:3] offset:32
	v_rcp_f32_e32 v38, v30
	s_waitcnt vmcnt(8)
	v_mov_b32_e32 v31, v90
	v_add_f32_e32 v36, v84, v85
	v_mov_b32_e32 v37, v82
	v_fma_f32 v26, -v30, v38, 1.0
	v_fmac_f32_e32 v38, v26, v38
	v_div_scale_f32 v26, vcc, 1.0, v34, 1.0
	v_mul_f32_e32 v46, v26, v38
	v_fma_f32 v27, -v30, v46, v26
	v_fmac_f32_e32 v46, v27, v38
	v_fma_f32 v47, -v30, v46, v26
	v_mov_b32_e32 v26, v77
	v_mov_b32_e32 v27, v78
	v_mov_b32_e32 v77, v79
	v_mov_b32_e32 v30, v89
	v_mov_b32_e32 v89, v91
	v_pk_add_f32 v[26:27], v[26:27], v[76:77]
	v_pk_add_f32 v[30:31], v[30:31], v[88:89]
	v_pk_add_f32 v[26:27], v[26:27], v[26:27] op_sel:[0,1] op_sel_hi:[1,0]
	v_pk_add_f32 v[30:31], v[30:31], v[30:31] op_sel:[0,1] op_sel_hi:[1,0]
	v_mov_b32_e32 v27, v80
	v_mov_b32_e32 v31, v81
	v_pk_add_f32 v[26:27], v[26:27], v[30:31]
	v_pk_add_f32 v[30:31], v[36:37], v[42:43]
	v_add_co_u32_e64 v22, s[2:3], s19, v22
	v_pk_add_f32 v[26:27], v[26:27], v[30:31]
	s_nop 0
	v_addc_co_u32_e64 v23, s[2:3], 0, v23, s[2:3]
	v_add_f32_e32 v26, v26, v27
	v_fmamk_f32 v26, v26, 0x3a800000, v39
	v_mul_f32_e32 v27, 0x4f800000, v26
	v_cmp_gt_f32_e64 s[2:3], s18, v26
	global_load_dwordx2 v[76:77], v[22:23], off
	global_load_dwordx2 v[54:55], v[22:23], off offset:512
	global_load_dwordx2 v[48:49], v[22:23], off offset:1024
	global_load_dwordx2 v[44:45], v[22:23], off offset:1536
	v_cndmask_b32_e64 v50, v26, v27, s[2:3]
	v_sqrt_f32_e32 v51, v50
	v_cndmask_b32_e64 v20, v63, v20, s[0:1]
	v_add_u32_e32 v26, -1, v51
	v_fma_f32 v27, -v26, v51, v50
	v_cmp_ge_f32_e64 s[4:5], 0, v27
	s_nop 1
	v_cndmask_b32_e64 v78, v51, v26, s[4:5]
	global_load_dwordx2 v[42:43], v[22:23], off offset:2048
	global_load_dwordx2 v[36:37], v[22:23], off offset:2560
	global_load_dwordx2 v[30:31], v[22:23], off offset:3072
	global_load_dwordx2 v[26:27], v[22:23], off offset:3584
	v_add_u32_e32 v22, 1, v51
	v_fma_f32 v23, -v22, v51, v50
	v_cmp_lt_f32_e64 s[4:5], 0, v23
	s_waitcnt vmcnt(14)
	v_mov_b32_e32 v51, v66
	v_cndmask_b32_e64 v22, v78, v22, s[4:5]
	v_mul_f32_e32 v23, 0x37800000, v22
	v_cndmask_b32_e64 v22, v22, v23, s[2:3]
	v_cmp_class_f32_e64 s[2:3], v50, v62
	s_nop 1
	v_cndmask_b32_e64 v23, v22, v50, s[2:3]
	v_div_fmas_f32 v22, v47, v38, v46
	v_mov_b32_e32 v46, v57
	v_mov_b32_e32 v47, v58
	v_mov_b32_e32 v57, v59
	v_mov_b32_e32 v50, v65
	v_mov_b32_e32 v65, v67
	v_pk_add_f32 v[46:47], v[46:47], v[56:57]
	v_pk_add_f32 v[50:51], v[50:51], v[64:65]
	v_pk_add_f32 v[46:47], v[46:47], v[46:47] op_sel:[0,1] op_sel_hi:[1,0]
	v_pk_add_f32 v[50:51], v[50:51], v[50:51] op_sel:[0,1] op_sel_hi:[1,0]
	s_waitcnt vmcnt(8)
	v_add_f32_e32 v56, v72, v73
	v_add_f32_e32 v58, v74, v75
	v_mov_b32_e32 v47, v68
	v_mov_b32_e32 v51, v69
	v_mov_b32_e32 v57, v70
	v_mov_b32_e32 v59, v71
	v_pk_add_f32 v[46:47], v[46:47], v[50:51]
	v_pk_add_f32 v[50:51], v[56:57], v[58:59]
	v_div_scale_f32 v78, s[2:3], v23, v23, 1.0
	v_pk_add_f32 v[46:47], v[46:47], v[50:51]
	v_rcp_f32_e32 v79, v78
	v_add_f32_e32 v46, v46, v47
	v_fmamk_f32 v46, v46, 0x3a800000, v39
	v_mul_f32_e32 v47, 0x4f800000, v46
	v_cmp_gt_f32_e64 s[2:3], s18, v46
	v_div_fixup_f32 v22, v22, v34, 1.0
	v_fma_f32 v34, -v78, v79, 1.0
	v_cndmask_b32_e64 v46, v46, v47, s[2:3]
	v_sqrt_f32_e32 v47, v46
	v_fmac_f32_e32 v79, v34, v79
	v_div_scale_f32 v34, vcc, 1.0, v23, 1.0
	v_mul_f32_e32 v38, v34, v79
	v_fma_f32 v50, -v78, v38, v34
	v_fmac_f32_e32 v38, v50, v79
	v_add_u32_e32 v50, -1, v47
	v_fma_f32 v51, -v50, v47, v46
	v_cmp_ge_f32_e64 s[4:5], 0, v51
	v_add_u32_e32 v51, 1, v47
	v_fma_f32 v34, -v78, v38, v34
	v_cndmask_b32_e64 v50, v47, v50, s[4:5]
	v_fma_f32 v47, -v51, v47, v46
	v_cmp_lt_f32_e64 s[4:5], 0, v47
	v_div_fmas_f32 v34, v34, v79, v38
	v_div_fixup_f32 v23, v34, v23, 1.0
	v_cndmask_b32_e64 v47, v50, v51, s[4:5]
	v_mul_f32_e32 v50, 0x37800000, v47
	v_cndmask_b32_e64 v47, v47, v50, s[2:3]
	v_cmp_class_f32_e64 s[2:3], v46, v62
	v_cndmask_b32_e64 v34, v63, v23, s[0:1]
	v_cndmask_b32_e64 v22, v63, v22, s[0:1]
	v_cndmask_b32_e64 v46, v47, v46, s[2:3]
	v_div_scale_f32 v47, s[2:3], v46, v46, 1.0
	v_rcp_f32_e32 v50, v47
	s_nop 0
	v_fma_f32 v23, -v47, v50, 1.0
	v_fmac_f32_e32 v50, v23, v50
	v_div_scale_f32 v23, vcc, 1.0, v46, 1.0
	v_mul_f32_e32 v38, v23, v50
	v_fma_f32 v51, -v47, v38, v23
	v_fmac_f32_e32 v38, v51, v50
	v_fma_f32 v23, -v47, v38, v23
	v_div_fmas_f32 v23, v23, v50, v38
	v_div_fixup_f32 v23, v23, v46, 1.0
	v_cndmask_b32_e64 v38, v63, v23, s[0:1]
	v_lshlrev_b32_e32 v64, 16, v24
	v_and_b32_e32 v65, 0xffff0000, v24
	v_add_co_u32_e32 v24, vcc, s20, v16
	v_lshlrev_b32_e32 v66, 16, v25
	v_and_b32_e32 v67, 0xffff0000, v25
	v_addc_co_u32_e32 v25, vcc, 0, v17, vcc
	v_lshlrev_b32_e32 v46, 16, v40
	v_and_b32_e32 v47, 0xffff0000, v40
	v_lshlrev_b32_e32 v40, 16, v41
	v_and_b32_e32 v41, 0xffff0000, v41
	v_lshlrev_b32_e32 v56, 16, v28
	v_and_b32_e32 v57, 0xffff0000, v28
	v_add_co_u32_e32 v28, vcc, s21, v16
	s_addk_i32 s15, 0x400
	v_lshlrev_b32_e32 v50, 16, v32
	v_and_b32_e32 v51, 0xffff0000, v32
	v_lshlrev_b32_e32 v32, 16, v33
	v_and_b32_e32 v33, 0xffff0000, v33
	v_lshlrev_b32_e32 v58, 16, v29
	v_and_b32_e32 v59, 0xffff0000, v29
	v_lshlrev_b32_e32 v68, 16, v92
	v_and_b32_e32 v69, 0xffff0000, v92
	v_lshlrev_b32_e32 v70, 16, v93
	v_and_b32_e32 v71, 0xffff0000, v93
	v_addc_co_u32_e32 v29, vcc, 0, v17, vcc
	v_lshlrev_b32_e32 v72, 16, v94
	v_and_b32_e32 v73, 0xffff0000, v94
	v_lshlrev_b32_e32 v74, 16, v95
	v_and_b32_e32 v75, 0xffff0000, v95
	v_lshlrev_b32_e32 v78, 16, v60
	v_and_b32_e32 v79, 0xffff0000, v60
	v_lshlrev_b32_e32 v60, 16, v61
	v_and_b32_e32 v61, 0xffff0000, v61
	v_lshlrev_b32_e32 v80, 16, v52
	v_and_b32_e32 v81, 0xffff0000, v52
	v_lshlrev_b32_e32 v52, 16, v53
	v_and_b32_e32 v53, 0xffff0000, v53
	s_waitcnt vmcnt(7)
	v_lshlrev_b32_e32 v82, 16, v76
	v_and_b32_e32 v83, 0xffff0000, v76
	v_lshlrev_b32_e32 v76, 16, v77
	v_and_b32_e32 v77, 0xffff0000, v77
	s_waitcnt vmcnt(6)
	v_lshlrev_b32_e32 v84, 16, v54
	v_and_b32_e32 v85, 0xffff0000, v54
	v_lshlrev_b32_e32 v54, 16, v55
	v_and_b32_e32 v55, 0xffff0000, v55
	s_waitcnt vmcnt(5)
	v_lshlrev_b32_e32 v86, 16, v48
	v_and_b32_e32 v87, 0xffff0000, v48
	v_lshlrev_b32_e32 v48, 16, v49
	v_and_b32_e32 v49, 0xffff0000, v49
	s_waitcnt vmcnt(4)
	v_lshlrev_b32_e32 v88, 16, v44
	v_and_b32_e32 v89, 0xffff0000, v44
	v_lshlrev_b32_e32 v44, 16, v45
	v_and_b32_e32 v45, 0xffff0000, v45
	s_waitcnt vmcnt(3)
	v_lshlrev_b32_e32 v90, 16, v42
	v_and_b32_e32 v91, 0xffff0000, v42
	v_lshlrev_b32_e32 v42, 16, v43
	v_and_b32_e32 v43, 0xffff0000, v43
	s_waitcnt vmcnt(2)
	v_lshlrev_b32_e32 v92, 16, v36
	v_and_b32_e32 v93, 0xffff0000, v36
	v_lshlrev_b32_e32 v36, 16, v37
	v_and_b32_e32 v37, 0xffff0000, v37
	s_waitcnt vmcnt(1)
	v_lshlrev_b32_e32 v94, 16, v30
	v_and_b32_e32 v95, 0xffff0000, v30
	v_lshlrev_b32_e32 v30, 16, v31
	v_and_b32_e32 v31, 0xffff0000, v31
	s_waitcnt vmcnt(0)
	v_lshlrev_b32_e32 v96, 16, v26
	v_and_b32_e32 v97, 0xffff0000, v26
	v_lshlrev_b32_e32 v26, 16, v27
	v_and_b32_e32 v27, 0xffff0000, v27
	v_pk_mul_f32 v[46:47], v[20:21], v[46:47] op_sel_hi:[0,1]
	v_pk_mul_f32 v[40:41], v[20:21], v[40:41] op_sel_hi:[0,1]
	s_add_u32 s16, s16, 0x10000
	v_add_co_u32_e32 v104, vcc, s22, v16
	v_pk_mul_f32 v[50:51], v[20:21], v[50:51] op_sel_hi:[0,1]
	v_pk_mul_f32 v[98:99], v[20:21], v[32:33] op_sel_hi:[0,1]
	v_pk_mul_f32 v[56:57], v[20:21], v[56:57] op_sel_hi:[0,1]
	v_pk_mul_f32 v[58:59], v[20:21], v[58:59] op_sel_hi:[0,1]
	v_pk_mul_f32 v[64:65], v[20:21], v[64:65] op_sel_hi:[0,1]
	v_pk_mul_f32 v[66:67], v[20:21], v[66:67] op_sel_hi:[0,1]
	v_pk_mul_f32 v[68:69], v[22:23], v[68:69] op_sel_hi:[0,1]
	v_pk_mul_f32 v[70:71], v[22:23], v[70:71] op_sel_hi:[0,1]
	v_pk_mul_f32 v[72:73], v[22:23], v[72:73] op_sel_hi:[0,1]
	v_pk_mul_f32 v[74:75], v[22:23], v[74:75] op_sel_hi:[0,1]
	v_pk_mul_f32 v[78:79], v[22:23], v[78:79] op_sel_hi:[0,1]
	v_pk_mul_f32 v[60:61], v[22:23], v[60:61] op_sel_hi:[0,1]
	v_pk_mul_f32 v[80:81], v[22:23], v[80:81] op_sel_hi:[0,1]
	v_pk_mul_f32 v[22:23], v[22:23], v[52:53] op_sel_hi:[0,1]
	v_pk_mul_f32 v[82:83], v[34:35], v[82:83] op_sel_hi:[0,1]
	v_pk_mul_f32 v[76:77], v[34:35], v[76:77] op_sel_hi:[0,1]
	v_pk_mul_f32 v[84:85], v[34:35], v[84:85] op_sel_hi:[0,1]
	v_pk_mul_f32 v[100:101], v[34:35], v[54:55] op_sel_hi:[0,1]
	v_pk_mul_f32 v[86:87], v[34:35], v[86:87] op_sel_hi:[0,1]
	v_pk_mul_f32 v[102:103], v[34:35], v[48:49] op_sel_hi:[0,1]
	v_pk_mul_f32 v[88:89], v[34:35], v[88:89] op_sel_hi:[0,1]
	v_pk_mul_f32 v[106:107], v[34:35], v[44:45] op_sel_hi:[0,1]
	v_pk_mul_f32 v[108:109], v[38:39], v[90:91] op_sel_hi:[0,1]
	v_pk_mul_f32 v[90:91], v[38:39], v[42:43] op_sel_hi:[0,1]
	v_pk_mul_f32 v[92:93], v[38:39], v[92:93] op_sel_hi:[0,1]
	v_pk_mul_f32 v[36:37], v[38:39], v[36:37] op_sel_hi:[0,1]
	v_pk_mul_f32 v[110:111], v[38:39], v[94:95] op_sel_hi:[0,1]
	v_pk_mul_f32 v[112:113], v[38:39], v[30:31] op_sel_hi:[0,1]
	v_pk_mul_f32 v[114:115], v[38:39], v[96:97] op_sel_hi:[0,1]
	v_pk_mul_f32 v[26:27], v[38:39], v[26:27] op_sel_hi:[0,1]
	v_pk_mul_f32 v[32:33], v[2:3], v[40:41]
	v_pk_mul_f32 v[30:31], v[0:1], v[46:47]
	s_addc_u32 s17, s17, 0
	v_addc_co_u32_e32 v105, vcc, 0, v17, vcc
	v_lshl_add_u64 v[18:19], v[18:19], 0, s[10:11]
	v_pk_mul_f32 v[42:43], v[6:7], v[98:99]
	v_pk_mul_f32 v[40:41], v[4:5], v[50:51]
	v_pk_mul_f32 v[46:47], v[10:11], v[58:59]
	v_pk_mul_f32 v[44:45], v[8:9], v[56:57]
	v_pk_mul_f32 v[50:51], v[14:15], v[66:67]
	v_pk_mul_f32 v[48:49], v[12:13], v[64:65]
	v_pk_mul_f32 v[54:55], v[2:3], v[70:71]
	v_pk_mul_f32 v[52:53], v[0:1], v[68:69]
	v_pk_mul_f32 v[58:59], v[6:7], v[74:75]
	v_pk_mul_f32 v[56:57], v[4:5], v[72:73]
	v_pk_mul_f32 v[66:67], v[10:11], v[60:61]
	v_pk_mul_f32 v[64:65], v[8:9], v[78:79]
	v_pk_mul_f32 v[70:71], v[14:15], v[22:23]
	v_pk_mul_f32 v[68:69], v[12:13], v[80:81]
	v_pk_mul_f32 v[74:75], v[2:3], v[76:77]
	v_pk_mul_f32 v[72:73], v[0:1], v[82:83]
	v_pk_mul_f32 v[78:79], v[6:7], v[100:101]
	v_pk_mul_f32 v[76:77], v[4:5], v[84:85]
	v_pk_mul_f32 v[82:83], v[10:11], v[102:103]
	v_pk_mul_f32 v[80:81], v[8:9], v[86:87]
	v_pk_mul_f32 v[86:87], v[14:15], v[106:107]
	v_pk_mul_f32 v[84:85], v[12:13], v[88:89]
	v_pk_mul_f32 v[90:91], v[2:3], v[90:91]
	v_pk_mul_f32 v[88:89], v[0:1], v[108:109]
	v_pk_mul_f32 v[94:95], v[6:7], v[36:37]
	v_pk_mul_f32 v[92:93], v[4:5], v[92:93]
	v_pk_mul_f32 v[98:99], v[10:11], v[112:113]
	v_pk_mul_f32 v[96:97], v[8:9], v[110:111]
	v_pk_mul_f32 v[102:103], v[14:15], v[26:27]
	v_pk_mul_f32 v[100:101], v[12:13], v[114:115]
	global_store_dwordx4 v[16:17], v[30:33], off nt
	global_store_dwordx4 v[16:17], v[40:43], off offset:1024 nt
	global_store_dwordx4 v[16:17], v[44:47], off offset:2048 nt
	global_store_dwordx4 v[16:17], v[48:51], off offset:3072 nt
	global_store_dwordx4 v[28:29], v[52:55], off offset:-4096 nt
	global_store_dwordx4 v[24:25], v[56:59], off offset:1024 nt
	global_store_dwordx4 v[24:25], v[64:67], off offset:2048 nt
	global_store_dwordx4 v[24:25], v[68:71], off offset:3072 nt
	global_store_dwordx4 v[28:29], v[72:75], off nt
	global_store_dwordx4 v[28:29], v[76:79], off offset:1024 nt
	global_store_dwordx4 v[28:29], v[80:83], off offset:2048 nt
	global_store_dwordx4 v[28:29], v[84:87], off offset:3072 nt
	global_store_dwordx4 v[104:105], v[88:91], off nt
	global_store_dwordx4 v[104:105], v[92:95], off offset:1024 nt
	global_store_dwordx4 v[104:105], v[96:99], off offset:2048 nt
	global_store_dwordx4 v[104:105], v[100:103], off offset:3072 nt
	s_cmp_ge_i32 s15, s14
	v_lshl_add_u64 v[16:17], v[16:17], 0, s[8:9]
	s_cbranch_scc0 .LBB0_1494
